# norm2+router phases: router bias parked in LDS (no global load per logit-loop trip); next 16-row x block prefetched during the top-k tail into the idle router fragment registers
# speedup vs baseline: 1.0050x; 1.0050x over previous
; #define LAS __attribute__((address_space(3)))
; template <int MODE>
; __device__ __forceinline__ void norm_phase(const MkArgs& a, LAS unsigned char* lds, const int l, const int wv) {
;     ...
;         if (rb == cb4) {
;             const int k4 = tid * 4;
;             const f32x4 g4 = *(const f32x4*)(gain + k4);
;             if constexpr (MODE != 3) {
;                 const float* sh_ = mod + ((size_t)l * 8 + b) * (6 * DM) + (MODE == 2 ? 3 * DM : 0);
;                 const f32x4 s4 = *(const f32x4*)(sh_ + k4), c4 = *(const f32x4*)(sh_ + DM + k4);
;                 *(LAS f32x4*)&tabA[k4] = (f32x4){g4[0] * (1.0f + c4[0]), g4[1] * (1.0f + c4[1]), g4[2] * (1.0f + c4[2]), g4[3] * (1.0f + c4[3])};
;                 *(LAS f32x4*)&tabB[k4] = s4;
;             } else *(LAS f32x4*)&tabA[k4] = g4;
;             if constexpr (MODE == 1 || MODE == 3) {
;                 const int lm_ = (MODE == 1) ? l - 1 : 1;
;                 *(LAS f32x4*)&tabG[k4] = *(const f32x4*)(mod + ((size_t)lm_ * 8 + b) * (6 * DM) + 5 * DM + k4);
;             }
;             __syncthreads();
;         }
;         float xv[64];
; #pragma unroll
;         for (int j = 0; j < 8; ++j) {
;             const int k = 256 * w + 32 * j + 8 * q;
;             const f32x4 v0 = *(const f32x4*)(xsrc + (size_t)t * DM + k), v1 = *(const f32x4*)(xsrc + (size_t)t * DM + k + 4);
;             xv[8 * j + 0] = v0[0]; xv[8 * j + 1] = v0[1]; xv[8 * j + 2] = v0[2]; xv[8 * j + 3] = v0[3];
;             xv[8 * j + 4] = v1[0]; xv[8 * j + 5] = v1[1]; xv[8 * j + 6] = v1[2]; xv[8 * j + 7] = v1[3];
;         }
;     ...
;         float ss = 0.f;
; #pragma unroll
;         for (int i = 0; i < 64; ++i) ss += xv[i] * xv[i];
;         ss += __shfl_xor(ss, 16); ss += __shfl_xor(ss, 32);
;         if (q == 0) ssp[w * 16 + r] = ss;
.LBB0_897:
	s_cmp_lg_u32 s29, s33
	s_cbranch_scc1 .LBB0_899
	global_load_dwordx4 v[0:3], v[80:81], off
	global_load_dwordx4 v[4:7], v[78:79], off
	global_load_dwordx4 v[8:11], v[74:75], off
	s_waitcnt vmcnt(2)
	v_pk_add_f32 v[2:3], v[2:3], 1.0 op_sel_hi:[1,0]
	v_pk_add_f32 v[0:1], v[0:1], 1.0 op_sel_hi:[1,0]
	s_waitcnt vmcnt(0)
	v_pk_mul_f32 v[2:3], v[10:11], v[2:3]
	v_pk_mul_f32 v[0:1], v[8:9], v[0:1]
	ds_write_b128 v116, v[4:7]
	ds_write_b128 v115, v[0:3]
	v_cmp_gt_u32_e32 vcc, 36, v64
	s_and_saveexec_b64 s[14:15], vcc
	v_mov_b32_e32 v4, v64
	v_ashrrev_i32_e32 v5, 31, v4
	v_cmp_gt_i32_e32 vcc, 4, v4
	v_lshl_add_u64 v[6:7], v[4:5], 2, s[52:53]
	v_mov_b32_e32 v5, v77
	v_lshl_add_u64 v[4:5], v[4:5], 2, s[56:57]
	v_lshl_add_u64 v[4:5], v[4:5], 0, -16
	v_cndmask_b32_e32 v5, v5, v7, vcc
	v_cndmask_b32_e32 v4, v4, v6, vcc
	global_load_dword v3, v[4:5], off
	v_lshlrev_b32_e32 v6, 2, v64
	s_waitcnt vmcnt(0)
	ds_write_b32 v6, v3 offset:27904
	s_or_b64 exec, exec, s[14:15]
	s_waitcnt lgkmcnt(0)
	s_barrier
.LBB0_899:
	s_lshl_b32 s30, s29, 4
	v_or_b32_e32 v82, s30, v148
	v_ashrrev_i32_e32 v83, 31, v82
	v_lshlrev_b64 v[0:1], 13, v[82:83]
	v_lshl_add_u64 v[0:1], v[68:69], 0, v[0:1]
	s_cmp_lg_u32 s29, s33
	s_cbranch_scc0 .Lmy_xld_0
	s_waitcnt vmcnt(0)
	v_mov_b64_e32 v[60:61], v[160:161]
	v_mov_b64_e32 v[62:63], v[162:163]
	v_mov_b64_e32 v[44:45], v[164:165]
	v_mov_b64_e32 v[46:47], v[166:167]
	v_mov_b64_e32 v[56:57], v[168:169]
	v_mov_b64_e32 v[58:59], v[170:171]
	v_mov_b64_e32 v[24:25], v[172:173]
	v_mov_b64_e32 v[26:27], v[174:175]
	v_mov_b64_e32 v[52:53], v[176:177]
	v_mov_b64_e32 v[54:55], v[178:179]
	v_mov_b64_e32 v[4:5], v[180:181]
	v_mov_b64_e32 v[6:7], v[182:183]
	v_mov_b64_e32 v[48:49], v[184:185]
	v_mov_b64_e32 v[50:51], v[186:187]
	v_mov_b64_e32 v[8:9], v[188:189]
	v_mov_b64_e32 v[10:11], v[190:191]
	v_mov_b64_e32 v[40:41], v[192:193]
	v_mov_b64_e32 v[42:43], v[194:195]
	v_mov_b64_e32 v[12:13], v[196:197]
	v_mov_b64_e32 v[14:15], v[198:199]
	v_mov_b64_e32 v[36:37], v[200:201]
	v_mov_b64_e32 v[38:39], v[202:203]
	v_mov_b64_e32 v[16:17], v[204:205]
	v_mov_b64_e32 v[18:19], v[206:207]
	v_mov_b64_e32 v[32:33], v[208:209]
	v_mov_b64_e32 v[34:35], v[210:211]
	v_mov_b64_e32 v[20:21], v[212:213]
	v_mov_b64_e32 v[22:23], v[214:215]
	v_mov_b64_e32 v[28:29], v[216:217]
	v_mov_b64_e32 v[30:31], v[218:219]
	v_mov_b64_e32 v[0:1], v[220:221]
	v_mov_b64_e32 v[2:3], v[222:223]
	s_branch .Lmy_xjn_0
.Lmy_xld_0:
	global_load_dwordx4 v[60:63], v[0:1], off
	global_load_dwordx4 v[44:47], v[0:1], off offset:16
	global_load_dwordx4 v[56:59], v[0:1], off offset:128
	global_load_dwordx4 v[24:27], v[0:1], off offset:144
	global_load_dwordx4 v[52:55], v[0:1], off offset:256
	global_load_dwordx4 v[4:7], v[0:1], off offset:272
	global_load_dwordx4 v[48:51], v[0:1], off offset:384
	global_load_dwordx4 v[8:11], v[0:1], off offset:400
	global_load_dwordx4 v[40:43], v[0:1], off offset:512
	global_load_dwordx4 v[12:15], v[0:1], off offset:528
	global_load_dwordx4 v[36:39], v[0:1], off offset:640
	global_load_dwordx4 v[16:19], v[0:1], off offset:656
	global_load_dwordx4 v[32:35], v[0:1], off offset:768
	global_load_dwordx4 v[20:23], v[0:1], off offset:784
	global_load_dwordx4 v[28:31], v[0:1], off offset:896
	s_nop 0
	global_load_dwordx4 v[0:3], v[0:1], off offset:912
.Lmy_xjn_0:
	s_waitcnt vmcnt(15)
	v_mul_f32_e32 v76, v61, v61
	v_fmac_f32_e32 v76, v60, v60
	v_fmac_f32_e32 v76, v62, v62
	v_fmac_f32_e32 v76, v63, v63
	s_waitcnt vmcnt(14)
	v_fmac_f32_e32 v76, v44, v44
	v_fmac_f32_e32 v76, v45, v45
	v_fmac_f32_e32 v76, v46, v46
	v_fmac_f32_e32 v76, v47, v47
	s_waitcnt vmcnt(13)
	v_fmac_f32_e32 v76, v56, v56
	v_fmac_f32_e32 v76, v57, v57
	v_fmac_f32_e32 v76, v58, v58
	v_fmac_f32_e32 v76, v59, v59
	s_waitcnt vmcnt(12)
	v_fmac_f32_e32 v76, v24, v24
	v_fmac_f32_e32 v76, v25, v25
	v_fmac_f32_e32 v76, v26, v26
	v_fmac_f32_e32 v76, v27, v27
	s_waitcnt vmcnt(11)
	v_fmac_f32_e32 v76, v52, v52
	v_fmac_f32_e32 v76, v53, v53
	v_fmac_f32_e32 v76, v54, v54
	v_fmac_f32_e32 v76, v55, v55
	s_waitcnt vmcnt(10)
	v_fmac_f32_e32 v76, v4, v4
	v_fmac_f32_e32 v76, v5, v5
	v_fmac_f32_e32 v76, v6, v6
	v_fmac_f32_e32 v76, v7, v7
	s_waitcnt vmcnt(9)
	v_fmac_f32_e32 v76, v48, v48
	v_fmac_f32_e32 v76, v49, v49
	v_fmac_f32_e32 v76, v50, v50
	v_fmac_f32_e32 v76, v51, v51
	s_waitcnt vmcnt(8)
	v_fmac_f32_e32 v76, v8, v8
	v_fmac_f32_e32 v76, v9, v9
	v_fmac_f32_e32 v76, v10, v10
	v_fmac_f32_e32 v76, v11, v11
	s_waitcnt vmcnt(7)
	v_fmac_f32_e32 v76, v40, v40
	v_fmac_f32_e32 v76, v41, v41
	v_fmac_f32_e32 v76, v42, v42
	v_fmac_f32_e32 v76, v43, v43
	s_waitcnt vmcnt(6)
	v_fmac_f32_e32 v76, v12, v12
	v_fmac_f32_e32 v76, v13, v13
	v_fmac_f32_e32 v76, v14, v14
	v_fmac_f32_e32 v76, v15, v15
	s_waitcnt vmcnt(5)
	v_fmac_f32_e32 v76, v36, v36
	v_fmac_f32_e32 v76, v37, v37
	v_fmac_f32_e32 v76, v38, v38
	v_fmac_f32_e32 v76, v39, v39
	s_waitcnt vmcnt(4)
	v_fmac_f32_e32 v76, v16, v16
	v_fmac_f32_e32 v76, v17, v17
	v_fmac_f32_e32 v76, v18, v18
	v_fmac_f32_e32 v76, v19, v19
	s_waitcnt vmcnt(3)
	v_fmac_f32_e32 v76, v32, v32
	v_fmac_f32_e32 v76, v33, v33
	v_fmac_f32_e32 v76, v34, v34
	v_fmac_f32_e32 v76, v35, v35
	s_waitcnt vmcnt(2)
	v_fmac_f32_e32 v76, v20, v20
	v_fmac_f32_e32 v76, v21, v21
	v_fmac_f32_e32 v76, v22, v22
	v_fmac_f32_e32 v76, v23, v23
	s_waitcnt vmcnt(1)
	v_fmac_f32_e32 v76, v28, v28
	v_fmac_f32_e32 v76, v29, v29
	v_fmac_f32_e32 v76, v30, v30
	v_fmac_f32_e32 v76, v31, v31
	s_waitcnt vmcnt(0)
	v_fmac_f32_e32 v76, v0, v0
	v_fmac_f32_e32 v76, v1, v1
	v_fmac_f32_e32 v76, v2, v2
	v_fmac_f32_e32 v76, v3, v3
	ds_bpermute_b32 v84, v149, v76
	s_waitcnt lgkmcnt(0)
	v_add_f32_e32 v76, v76, v84
	ds_bpermute_b32 v84, v150, v76
	s_and_saveexec_b64 s[12:13], s[8:9]
	s_cbranch_execz .LBB0_901
	v_readlane_b32 s14, v252, 39
	s_waitcnt lgkmcnt(0)
	v_add_f32_e32 v76, v76, v84
	v_add_u32_e32 v84, s14, v151
	ds_write_b32 v84, v76

; template <int MODE>
; __device__ __forceinline__ void norm_phase(const MkArgs& a, LAS unsigned char* lds, const int l, const int wv) {
;     ...
;         float xv[64];
; #pragma unroll
;         for (int j = 0; j < 8; ++j) {
;             const int k = 256 * w + 32 * j + 8 * q;
;             const f32x4 v0 = *(const f32x4*)(xsrc + (size_t)t * DM + k), v1 = *(const f32x4*)(xsrc + (size_t)t * DM + k + 4);
;             xv[8 * j + 0] = v0[0]; xv[8 * j + 1] = v0[1]; xv[8 * j + 2] = v0[2]; xv[8 * j + 3] = v0[3];
;             xv[8 * j + 4] = v1[0]; xv[8 * j + 5] = v1[1]; xv[8 * j + 6] = v1[2]; xv[8 * j + 7] = v1[3];
;         }
;     ...
;             for (int o = tid; o < 16 * 36; o += 512) {
;                 const int rr = o / 36, c = o % 36; float s = 0.f;
; #pragma unroll
;                 for (int i = 0; i < 8; ++i) s += part[(i * 16 + rr) * 48 + c];
;                 lgt[o] = s + (c < 4 ? a.in[12][l * 4 + c] : a.in[14][l * 32 + c - 4]);
;             }
.LBB0_903:
	s_mov_b32 s16, 0x38e38e39
	v_mul_hi_i32 v1, v2, s16
	v_lshrrev_b32_e32 v3, 31, v1
	v_ashrrev_i32_e32 v1, 3, v1
	v_add_u32_e32 v1, v1, v3
	s_movk_i32 s16, 0xffdc
	v_mad_u64_u32 v[4:5], s[16:17], v1, s16, v[2:3]
	v_mad_u64_u32 v[6:7], s[16:17], v1, 48, v[0:1]
	ds_read2st64_b32 v[8:9], v6 offset0:4 offset1:16
	v_ashrrev_i32_e32 v5, 31, v4
	v_cmp_gt_i32_e32 vcc, 4, v4
	s_waitcnt lgkmcnt(0)
	v_add_f32_e32 v1, 0, v8
	v_add_f32_e32 v1, v1, v9
	ds_read2st64_b32 v[8:9], v6 offset0:28 offset1:40
	s_waitcnt lgkmcnt(0)
	v_add_f32_e32 v1, v1, v8
	v_add_f32_e32 v1, v1, v9
	ds_read2st64_b32 v[8:9], v6 offset0:52 offset1:64
	ds_read2st64_b32 v[6:7], v6 offset0:76 offset1:88
	s_waitcnt lgkmcnt(1)
	v_add_f32_e32 v1, v1, v8
	v_add_f32_e32 v1, v1, v9
	s_waitcnt lgkmcnt(0)
	v_add_f32_e32 v1, v1, v6
	v_add_f32_e32 v1, v1, v7
	v_lshlrev_b32_e32 v4, 2, v4
	ds_read_b32 v3, v4 offset:27904
	v_cmp_lt_i32_e32 vcc, 63, v2
	s_or_b64 s[14:15], vcc, s[14:15]
	s_waitcnt lgkmcnt(0)
	v_add_f32_e32 v1, v1, v3
	ds_write_b32 v0, v1 offset:25600
	v_add_u32_e32 v1, 0x200, v2
	v_add_u32_e32 v0, 0x800, v0
	v_mov_b32_e32 v2, v1
	s_andn2_b64 exec, exec, s[14:15]
	s_cbranch_execnz .LBB0_903
.LBB0_904:
	s_or_b64 exec, exec, s[12:13]
	s_add_i32 s99, s29, 1
	s_cmp_eq_u32 s99, s28
	s_cbranch_scc1 .Lmy_xpf_skip_0
	s_lshl_b32 s99, s99, 4
	v_or_b32_e32 v224, s99, v148
	v_ashrrev_i32_e32 v225, 31, v224
	v_lshlrev_b64 v[224:225], 13, v[224:225]
	v_lshl_add_u64 v[224:225], v[68:69], 0, v[224:225]
	global_load_dwordx4 v[160:163], v[224:225], off
	global_load_dwordx4 v[164:167], v[224:225], off offset:16
	global_load_dwordx4 v[168:171], v[224:225], off offset:128
	global_load_dwordx4 v[172:175], v[224:225], off offset:144
	global_load_dwordx4 v[176:179], v[224:225], off offset:256
	global_load_dwordx4 v[180:183], v[224:225], off offset:272
	global_load_dwordx4 v[184:187], v[224:225], off offset:384
	global_load_dwordx4 v[188:191], v[224:225], off offset:400
	global_load_dwordx4 v[192:195], v[224:225], off offset:512
	global_load_dwordx4 v[196:199], v[224:225], off offset:528
	global_load_dwordx4 v[200:203], v[224:225], off offset:640
	global_load_dwordx4 v[204:207], v[224:225], off offset:656
	global_load_dwordx4 v[208:211], v[224:225], off offset:768
	global_load_dwordx4 v[212:215], v[224:225], off offset:784
	global_load_dwordx4 v[216:219], v[224:225], off offset:896
	global_load_dwordx4 v[220:223], v[224:225], off offset:912
; #define LAS __attribute__((address_space(3)))
; template <int MODE>
; __device__ __forceinline__ void norm_phase(const MkArgs& a, LAS unsigned char* lds, const int l, const int wv) {
;     ...
;             if (tid < 16) {
;                 const LAS float* sl = lgt + tid * 36; const int tt = rb * 16 + tid;
;                 int grp = 0; float m = sl[0];
;                 for (int g = 1; g < 4; ++g) if (sl[g] > m) { m = sl[g]; grp = g; }
;                 float se = 0.f;
;                 for (int g = 0; g < 4; ++g) se += __builtin_amdgcn_exp2f((sl[g] - m) * 1.4426950408889634f);
;                 const float pg = 1.0f / se;
;                 const LAS float* lgp = sl + 4 + grp * 8;
;                 const f32x4 l0 = *(const LAS f32x4*)lgp, l1 = *(const LAS f32x4*)(lgp + 4);
;                 const float lv[8] = {l0[0], l0[1], l0[2], l0[3], l1[0], l1[1], l1[2], l1[3]};
;                 int i0 = 0; float v0 = lv[0];
; #pragma unroll
;                 for (int jx = 1; jx < 8; ++jx) if (lv[jx] > v0) { v0 = lv[jx]; i0 = jx; }
;                 int i1 = -1; float v1 = 0.f;
; #pragma unroll
;                 for (int jx = 0; jx < 8; ++jx) if (jx != i0 && (i1 < 0 || lv[jx] > v1)) { v1 = lv[jx]; i1 = jx; }
;                 const float e1 = __builtin_amdgcn_exp2f((v1 - v0) * 1.4426950408889634f);
;                 const float p0 = 1.0f / (1.0f + e1), p1 = e1 / (1.0f + e1);
;                 float* tokw = (float*)(ws + WS_TOKW);
;                 tokw[2 * tt] = pg * p0; tokw[2 * tt + 1] = pg * p1;
;                 const int ai = ((rb & 3) * 16 + tid) * 2;
;                 rexp[ai] = grp * 8 + i0; rexp[ai + 1] = grp * 8 + i1;
.Lmy_xpf_skip_0:
	s_waitcnt lgkmcnt(0)
	s_barrier
	s_and_saveexec_b64 s[24:25], s[10:11]
	s_cbranch_execz .LBB0_906
	ds_read_b128 v[0:3], v153 offset:25600
	s_waitcnt lgkmcnt(0)
	v_cmp_gt_f32_e32 vcc, v1, v0
	s_nop 1
	v_cndmask_b32_e32 v4, v0, v1, vcc
	v_cmp_gt_f32_e64 s[12:13], v2, v4
	s_nop 1
	v_cndmask_b32_e64 v4, v4, v2, s[12:13]
	v_cmp_gt_f32_e64 s[14:15], v3, v4
	s_nop 1
	v_cndmask_b32_e64 v8, v4, v3, s[14:15]
	v_sub_f32_e32 v0, v0, v8
	v_sub_f32_e32 v1, v1, v8
	v_mul_f32_e32 v0, 0x3fb8aa3b, v0
	v_exp_f32_e32 v9, v0
	v_mul_f32_e32 v0, 0x3fb8aa3b, v1
	v_exp_f32_e32 v10, v0
	v_sub_f32_e32 v0, v2, v8
	v_mul_f32_e32 v0, 0x3fb8aa3b, v0
	v_exp_f32_e32 v11, v0
	v_cndmask_b32_e64 v0, 0, 8, vcc
	v_cndmask_b32_e64 v0, v0, 16, s[12:13]
	v_cndmask_b32_e64 v12, v0, 24, s[14:15]
	v_lshl_add_u32 v0, v12, 2, v153
	ds_read_b128 v[4:7], v0 offset:25616
	v_sub_f32_e32 v1, v3, v8
	v_mul_f32_e32 v1, 0x3fb8aa3b, v1
	v_exp_f32_e32 v8, v1
	ds_read_b128 v[0:3], v0 offset:25632
	s_waitcnt lgkmcnt(1)
	v_cmp_gt_f32_e32 vcc, v5, v4
	v_add_f32_e32 v9, 0, v9
	v_add_f32_e32 v9, v10, v9
	v_cndmask_b32_e32 v14, v4, v5, vcc
	v_cmp_gt_f32_e64 s[12:13], v6, v14
	v_cndmask_b32_e64 v13, 0, 1, vcc
	v_add_f32_e32 v9, v11, v9
	v_cndmask_b32_e64 v14, v14, v6, s[12:13]
	v_cndmask_b32_e64 v13, v13, 2, s[12:13]
	v_cmp_gt_f32_e64 s[12:13], v7, v14
	v_add_f32_e32 v8, v8, v9
	s_nop 0
	v_cndmask_b32_e64 v14, v14, v7, s[12:13]
	v_cndmask_b32_e64 v13, v13, 3, s[12:13]
	s_waitcnt lgkmcnt(0)
	v_cmp_gt_f32_e64 s[12:13], v0, v14
	s_nop 1
	v_cndmask_b32_e64 v14, v14, v0, s[12:13]
	v_cndmask_b32_e64 v13, v13, 4, s[12:13]
	v_cmp_gt_f32_e64 s[12:13], v1, v14
	s_nop 1
	v_cndmask_b32_e64 v14, v14, v1, s[12:13]
	v_cndmask_b32_e64 v13, v13, 5, s[12:13]
	v_cmp_gt_f32_e64 s[12:13], v2, v14
	s_nop 1
	v_cndmask_b32_e64 v14, v14, v2, s[12:13]
	v_cndmask_b32_e64 v13, v13, 6, s[12:13]
	v_cmp_ngt_f32_e64 s[14:15], v3, v14
	s_nop 1
	v_cndmask_b32_e64 v13, 7, v13, s[14:15]
	v_cmp_eq_u32_e64 s[16:17], 0, v13
	v_cmp_ne_u32_e64 s[18:19], 1, v13
	s_or_b64 s[16:17], s[16:17], vcc
	s_and_b64 vcc, s[18:19], s[16:17]
	v_cndmask_b32_e32 v4, v4, v5, vcc
	v_cndmask_b32_e64 v9, 0, 1, vcc
	v_cmp_gt_f32_e32 vcc, v6, v4
	s_nop 1
	v_cndmask_b32_e64 v5, v9, 2, vcc
	v_cndmask_b32_e32 v6, v4, v6, vcc
	v_cmp_eq_u32_e32 vcc, 2, v13
	s_nop 1
	v_cndmask_b32_e32 v4, v6, v4, vcc
	v_cndmask_b32_e32 v9, v5, v9, vcc
	v_cmp_gt_f32_e32 vcc, v7, v4
	s_nop 1
	v_cndmask_b32_e64 v9, v9, 3, vcc
	v_cndmask_b32_e32 v4, v4, v7, vcc
	v_cmp_eq_u32_e32 vcc, 3, v13
	s_nop 1
	v_cndmask_b32_e32 v6, v4, v6, vcc
	v_cndmask_b32_e32 v5, v9, v5, vcc
	v_cmp_gt_f32_e32 vcc, v0, v6
	s_nop 1
	v_cndmask_b32_e64 v5, v5, 4, vcc
	v_cndmask_b32_e32 v0, v6, v0, vcc
	v_cmp_eq_u32_e32 vcc, 4, v13
	s_nop 1
	v_cndmask_b32_e32 v4, v0, v4, vcc
	v_cndmask_b32_e32 v6, v5, v9, vcc
	v_cmp_gt_f32_e32 vcc, v1, v4
	s_nop 1
	v_cndmask_b32_e64 v6, v6, 5, vcc
	v_cndmask_b32_e32 v1, v4, v1, vcc
	v_cmp_eq_u32_e32 vcc, 5, v13
	s_nop 1
	v_cndmask_b32_e32 v0, v1, v0, vcc
	v_cndmask_b32_e32 v4, v6, v5, vcc
	v_cmp_gt_f32_e32 vcc, v2, v0
	s_nop 1
	v_cndmask_b32_e64 v1, v4, 6, vcc
	v_cndmask_b32_e32 v2, v0, v2, vcc
	s_and_b64 vcc, s[12:13], s[14:15]
	v_div_scale_f32 v5, s[12:13], v8, v8, 1.0
	v_cndmask_b32_e32 v0, v2, v0, vcc
	v_rcp_f32_e32 v6, v5
	v_cndmask_b32_e32 v4, v1, v4, vcc
	v_cmp_gt_f32_e32 vcc, v3, v0
	s_nop 1
	v_cndmask_b32_e64 v2, v4, 7, vcc
	s_and_b64 vcc, s[14:15], vcc
	v_cndmask_b32_e64 v4, v3, v14, s[14:15]
	v_cndmask_b32_e32 v0, v0, v3, vcc
	v_cndmask_b32_e64 v7, v1, v2, s[14:15]
	v_fma_f32 v1, -v5, v6, 1.0
	v_sub_f32_e32 v0, v0, v4
	v_fmac_f32_e32 v6, v1, v6
	v_div_scale_f32 v1, vcc, 1.0, v8, 1.0
	v_mul_f32_e32 v0, 0x3fb8aa3b, v0
	v_mul_f32_e32 v2, v1, v6
	v_exp_f32_e32 v4, v0
	v_fma_f32 v3, -v5, v2, v1
	v_fmac_f32_e32 v2, v3, v6
	v_fma_f32 v1, -v5, v2, v1
	v_div_fmas_f32 v0, v1, v6, v2
	v_add_f32_e32 v1, 1.0, v4
	v_div_scale_f32 v5, s[12:13], v1, v1, v4
	v_rcp_f32_e32 v6, v5
	v_div_fixup_f32 v0, v0, v8, 1.0
	v_add_lshl_u32 v2, s30, v64, 1
	v_readlane_b32 s12, v252, 41
	v_fma_f32 v8, -v5, v6, 1.0
	v_fmac_f32_e32 v6, v8, v6
	v_div_scale_f32 v8, vcc, v4, v1, v4
	v_mul_f32_e32 v9, v8, v6
	v_fma_f32 v10, -v5, v9, v8
	v_ashrrev_i32_e32 v3, 31, v2
	v_readlane_b32 s13, v252, 42
	v_fmac_f32_e32 v9, v10, v6
	v_fma_f32 v5, -v5, v9, v8
	v_lshl_add_u64 v[2:3], v[2:3], 2, s[12:13]
	v_div_scale_f32 v8, s[12:13], v1, v1, 1.0
	v_rcp_f32_e32 v10, v8
	v_div_fmas_f32 v5, v5, v6, v9
	v_div_fixup_f32 v5, v5, v1, v4
	s_and_b32 s12, s30, 48
	v_fma_f32 v4, -v8, v10, 1.0
	v_fmac_f32_e32 v10, v4, v10
	v_div_scale_f32 v4, vcc, 1.0, v1, 1.0
	v_mul_f32_e32 v6, v4, v10
	v_fma_f32 v9, -v8, v6, v4
	v_fmac_f32_e32 v6, v9, v10
	v_fma_f32 v4, -v8, v6, v4
	v_div_fmas_f32 v4, v4, v10, v6
	v_div_fixup_f32 v4, v4, v1, 1.0
	v_pk_mul_f32 v[0:1], v[0:1], v[4:5] op_sel_hi:[0,1]
	global_store_dwordx2 v[2:3], v[0:1], off
	v_add_u32_e32 v1, s12, v64
	v_or_b32_e32 v0, v13, v12
	v_lshl_add_u32 v2, v1, 3, 0
	v_add_u32_e32 v1, v7, v12
	ds_write_b64 v2, v[0:1] offset:28672

; #define LAS __attribute__((address_space(3)))
; template <int MODE>
; __device__ __forceinline__ void norm_phase(const MkArgs& a, LAS unsigned char* lds, const int l, const int wv) {
;     ...
;         if (rb == cb4) {
;             const int k4 = tid * 4;
;             const f32x4 g4 = *(const f32x4*)(gain + k4);
;             if constexpr (MODE != 3) {
;                 const float* sh_ = mod + ((size_t)l * 8 + b) * (6 * DM) + (MODE == 2 ? 3 * DM : 0);
;                 const f32x4 s4 = *(const f32x4*)(sh_ + k4), c4 = *(const f32x4*)(sh_ + DM + k4);
;                 *(LAS f32x4*)&tabA[k4] = (f32x4){g4[0] * (1.0f + c4[0]), g4[1] * (1.0f + c4[1]), g4[2] * (1.0f + c4[2]), g4[3] * (1.0f + c4[3])};
;                 *(LAS f32x4*)&tabB[k4] = s4;
;             } else *(LAS f32x4*)&tabA[k4] = g4;
;             if constexpr (MODE == 1 || MODE == 3) {
;                 const int lm_ = (MODE == 1) ? l - 1 : 1;
;                 *(LAS f32x4*)&tabG[k4] = *(const f32x4*)(mod + ((size_t)lm_ * 8 + b) * (6 * DM) + 5 * DM + k4);
;             }
;             __syncthreads();
;         }
;         float xv[64];
; #pragma unroll
;         for (int j = 0; j < 8; ++j) {
;             const int k = 256 * w + 32 * j + 8 * q;
;             const f32x4 v0 = *(const f32x4*)(xsrc + (size_t)t * DM + k), v1 = *(const f32x4*)(xsrc + (size_t)t * DM + k + 4);
;             xv[8 * j + 0] = v0[0]; xv[8 * j + 1] = v0[1]; xv[8 * j + 2] = v0[2]; xv[8 * j + 3] = v0[3];
;             xv[8 * j + 4] = v1[0]; xv[8 * j + 5] = v1[1]; xv[8 * j + 6] = v1[2]; xv[8 * j + 7] = v1[3];
;         }
.LBB0_1969:
	s_cmp_lg_u32 s33, s0
	s_cbranch_scc1 .LBB0_1971
	global_load_dwordx4 v[0:3], v[80:81], off
	global_load_dwordx4 v[4:7], v[78:79], off
	global_load_dwordx4 v[8:11], v[68:69], off
	s_waitcnt vmcnt(2)
	v_pk_add_f32 v[2:3], v[2:3], 1.0 op_sel_hi:[1,0]
	v_pk_add_f32 v[0:1], v[0:1], 1.0 op_sel_hi:[1,0]
	s_waitcnt vmcnt(0)
	v_pk_mul_f32 v[2:3], v[10:11], v[2:3]
	v_pk_mul_f32 v[0:1], v[8:9], v[0:1]
	ds_write_b128 v121, v[4:7]
	ds_write_b128 v120, v[0:3]
	v_cmp_gt_u32_e32 vcc, 36, v64
	s_and_saveexec_b64 s[14:15], vcc
	v_mov_b32_e32 v4, v64
	v_ashrrev_i32_e32 v5, 31, v4
	v_cmp_gt_i32_e32 vcc, 4, v4
	s_mov_b64 s[16:17], 0x70
	v_lshl_add_u64 v[6:7], v[4:5], 2, s[52:53]
	v_mov_b32_e32 v5, v77
	v_lshl_add_u64 v[4:5], v[4:5], 2, s[56:57]
	v_lshl_add_u64 v[6:7], v[6:7], 0, 16
	v_lshl_add_u64 v[4:5], v[4:5], 0, s[16:17]
	v_cndmask_b32_e32 v5, v5, v7, vcc
	v_cndmask_b32_e32 v4, v4, v6, vcc
	global_load_dword v3, v[4:5], off
	v_lshlrev_b32_e32 v6, 2, v64
	s_waitcnt vmcnt(0)
	ds_write_b32 v6, v3 offset:27904
	s_or_b64 exec, exec, s[14:15]
	s_waitcnt lgkmcnt(0)
	s_barrier
.LBB0_1971:
	s_lshl_b32 s1, s33, 4
	v_or_b32_e32 v82, s1, v115
	v_ashrrev_i32_e32 v83, 31, v82
	v_lshlrev_b64 v[0:1], 13, v[82:83]
	v_lshl_add_u64 v[0:1], v[72:73], 0, v[0:1]
	s_cmp_lg_u32 s33, s0
	s_cbranch_scc0 .Lmy_xld_1
	s_waitcnt vmcnt(0)
	v_mov_b64_e32 v[60:61], v[160:161]
	v_mov_b64_e32 v[62:63], v[162:163]
	v_mov_b64_e32 v[44:45], v[164:165]
	v_mov_b64_e32 v[46:47], v[166:167]
	v_mov_b64_e32 v[56:57], v[168:169]
	v_mov_b64_e32 v[58:59], v[170:171]
	v_mov_b64_e32 v[24:25], v[172:173]
	v_mov_b64_e32 v[26:27], v[174:175]
	v_mov_b64_e32 v[52:53], v[176:177]
	v_mov_b64_e32 v[54:55], v[178:179]
	v_mov_b64_e32 v[4:5], v[180:181]
	v_mov_b64_e32 v[6:7], v[182:183]
	v_mov_b64_e32 v[48:49], v[184:185]
	v_mov_b64_e32 v[50:51], v[186:187]
	v_mov_b64_e32 v[8:9], v[188:189]
	v_mov_b64_e32 v[10:11], v[190:191]
	v_mov_b64_e32 v[40:41], v[192:193]
	v_mov_b64_e32 v[42:43], v[194:195]
	v_mov_b64_e32 v[12:13], v[196:197]
	v_mov_b64_e32 v[14:15], v[198:199]
	v_mov_b64_e32 v[36:37], v[200:201]
	v_mov_b64_e32 v[38:39], v[202:203]
	v_mov_b64_e32 v[16:17], v[204:205]
	v_mov_b64_e32 v[18:19], v[206:207]
	v_mov_b64_e32 v[32:33], v[208:209]
	v_mov_b64_e32 v[34:35], v[210:211]
	v_mov_b64_e32 v[20:21], v[212:213]
	v_mov_b64_e32 v[22:23], v[214:215]
	v_mov_b64_e32 v[28:29], v[216:217]
	v_mov_b64_e32 v[30:31], v[218:219]
	v_mov_b64_e32 v[0:1], v[220:221]
	v_mov_b64_e32 v[2:3], v[222:223]
	s_branch .Lmy_xjn_1

; template <int MODE>
; __device__ __forceinline__ void norm_phase(const MkArgs& a, LAS unsigned char* lds, const int l, const int wv) {
;     ...
;         float ss = 0.f;
; #pragma unroll
;         for (int i = 0; i < 64; ++i) ss += xv[i] * xv[i];
;         ss += __shfl_xor(ss, 16); ss += __shfl_xor(ss, 32);
;         if (q == 0) ssp[w * 16 + r] = ss;
.Lmy_xjn_1:
	s_waitcnt vmcnt(15)
	v_mul_f32_e32 v76, v61, v61
	v_fmac_f32_e32 v76, v60, v60
	v_fmac_f32_e32 v76, v62, v62
	v_fmac_f32_e32 v76, v63, v63
	s_waitcnt vmcnt(14)
	v_fmac_f32_e32 v76, v44, v44
	v_fmac_f32_e32 v76, v45, v45
	v_fmac_f32_e32 v76, v46, v46
	v_fmac_f32_e32 v76, v47, v47
	s_waitcnt vmcnt(13)
	v_fmac_f32_e32 v76, v56, v56
	v_fmac_f32_e32 v76, v57, v57
	v_fmac_f32_e32 v76, v58, v58
	v_fmac_f32_e32 v76, v59, v59
	s_waitcnt vmcnt(12)
	v_fmac_f32_e32 v76, v24, v24
	v_fmac_f32_e32 v76, v25, v25
	v_fmac_f32_e32 v76, v26, v26
	v_fmac_f32_e32 v76, v27, v27
	s_waitcnt vmcnt(11)
	v_fmac_f32_e32 v76, v52, v52
	v_fmac_f32_e32 v76, v53, v53
	v_fmac_f32_e32 v76, v54, v54
	v_fmac_f32_e32 v76, v55, v55
	s_waitcnt vmcnt(10)
	v_fmac_f32_e32 v76, v4, v4
	v_fmac_f32_e32 v76, v5, v5
	v_fmac_f32_e32 v76, v6, v6
	v_fmac_f32_e32 v76, v7, v7
	s_waitcnt vmcnt(9)
	v_fmac_f32_e32 v76, v48, v48
	v_fmac_f32_e32 v76, v49, v49
	v_fmac_f32_e32 v76, v50, v50
	v_fmac_f32_e32 v76, v51, v51
	s_waitcnt vmcnt(8)
	v_fmac_f32_e32 v76, v8, v8
	v_fmac_f32_e32 v76, v9, v9
	v_fmac_f32_e32 v76, v10, v10
	v_fmac_f32_e32 v76, v11, v11
	s_waitcnt vmcnt(7)
	v_fmac_f32_e32 v76, v40, v40
	v_fmac_f32_e32 v76, v41, v41
	v_fmac_f32_e32 v76, v42, v42
	v_fmac_f32_e32 v76, v43, v43
	s_waitcnt vmcnt(6)
	v_fmac_f32_e32 v76, v12, v12
	v_fmac_f32_e32 v76, v13, v13
	v_fmac_f32_e32 v76, v14, v14
	v_fmac_f32_e32 v76, v15, v15
	s_waitcnt vmcnt(5)
	v_fmac_f32_e32 v76, v36, v36
	v_fmac_f32_e32 v76, v37, v37
	v_fmac_f32_e32 v76, v38, v38
	v_fmac_f32_e32 v76, v39, v39
	s_waitcnt vmcnt(4)
	v_fmac_f32_e32 v76, v16, v16
	v_fmac_f32_e32 v76, v17, v17
	v_fmac_f32_e32 v76, v18, v18
	v_fmac_f32_e32 v76, v19, v19
	s_waitcnt vmcnt(3)
	v_fmac_f32_e32 v76, v32, v32
	v_fmac_f32_e32 v76, v33, v33
	v_fmac_f32_e32 v76, v34, v34
	v_fmac_f32_e32 v76, v35, v35
	s_waitcnt vmcnt(2)
	v_fmac_f32_e32 v76, v20, v20
	v_fmac_f32_e32 v76, v21, v21
	v_fmac_f32_e32 v76, v22, v22
	v_fmac_f32_e32 v76, v23, v23
	s_waitcnt vmcnt(1)
	v_fmac_f32_e32 v76, v28, v28
	v_fmac_f32_e32 v76, v29, v29
	v_fmac_f32_e32 v76, v30, v30
	v_fmac_f32_e32 v76, v31, v31
	s_waitcnt vmcnt(0)
	v_fmac_f32_e32 v76, v0, v0
	v_fmac_f32_e32 v76, v1, v1
	v_fmac_f32_e32 v76, v2, v2
	v_fmac_f32_e32 v76, v3, v3
	ds_bpermute_b32 v84, v116, v76
	s_waitcnt lgkmcnt(0)
	v_add_f32_e32 v76, v76, v84
	ds_bpermute_b32 v84, v117, v76
	s_and_saveexec_b64 s[12:13], s[4:5]
	s_cbranch_execz .LBB0_1973
	s_waitcnt lgkmcnt(0)
	v_add_f32_e32 v76, v76, v84
	v_add_u32_e32 v84, s26, v118
	ds_write_b32 v84, v76

; template <int MODE>
; __device__ __forceinline__ void norm_phase(const MkArgs& a, LAS unsigned char* lds, const int l, const int wv) {
;     ...
;         float xv[64];
; #pragma unroll
;         for (int j = 0; j < 8; ++j) {
;             const int k = 256 * w + 32 * j + 8 * q;
;             const f32x4 v0 = *(const f32x4*)(xsrc + (size_t)t * DM + k), v1 = *(const f32x4*)(xsrc + (size_t)t * DM + k + 4);
;             xv[8 * j + 0] = v0[0]; xv[8 * j + 1] = v0[1]; xv[8 * j + 2] = v0[2]; xv[8 * j + 3] = v0[3];
;             xv[8 * j + 4] = v1[0]; xv[8 * j + 5] = v1[1]; xv[8 * j + 6] = v1[2]; xv[8 * j + 7] = v1[3];
;         }
;     ...
;             for (int o = tid; o < 16 * 36; o += 512) {
;                 const int rr = o / 36, c = o % 36; float s = 0.f;
; #pragma unroll
;                 for (int i = 0; i < 8; ++i) s += part[(i * 16 + rr) * 48 + c];
;                 lgt[o] = s + (c < 4 ? a.in[12][l * 4 + c] : a.in[14][l * 32 + c - 4]);
;             }
.LBB0_1975:
	s_mov_b32 s16, 0x38e38e39
	v_mul_hi_i32 v1, v2, s16
	v_lshrrev_b32_e32 v3, 31, v1
	v_ashrrev_i32_e32 v1, 3, v1
	v_add_u32_e32 v1, v1, v3
	s_movk_i32 s16, 0xffdc
	v_mad_u64_u32 v[4:5], s[16:17], v1, s16, v[2:3]
	v_mad_u64_u32 v[6:7], s[16:17], v1, 48, v[0:1]
	ds_read2st64_b32 v[8:9], v6 offset0:4 offset1:16
	v_ashrrev_i32_e32 v5, 31, v4
	v_cmp_gt_i32_e32 vcc, 4, v4
	s_mov_b64 s[16:17], 0x70
	s_waitcnt lgkmcnt(0)
	v_add_f32_e32 v1, 0, v8
	v_add_f32_e32 v1, v1, v9
	ds_read2st64_b32 v[8:9], v6 offset0:28 offset1:40
	s_waitcnt lgkmcnt(0)
	v_add_f32_e32 v1, v1, v8
	v_add_f32_e32 v1, v1, v9
	ds_read2st64_b32 v[8:9], v6 offset0:52 offset1:64
	ds_read2st64_b32 v[6:7], v6 offset0:76 offset1:88
	s_waitcnt lgkmcnt(1)
	v_add_f32_e32 v1, v1, v8
	v_add_f32_e32 v1, v1, v9
	s_waitcnt lgkmcnt(0)
	v_add_f32_e32 v1, v1, v6
	v_add_f32_e32 v1, v1, v7
	v_lshlrev_b32_e32 v4, 2, v4
	ds_read_b32 v3, v4 offset:27904
	v_cmp_lt_i32_e32 vcc, 63, v2
	s_or_b64 s[14:15], vcc, s[14:15]
	s_waitcnt lgkmcnt(0)
	v_add_f32_e32 v1, v1, v3
	ds_write_b32 v0, v1 offset:25600
	v_add_u32_e32 v1, 0x200, v2
	v_add_u32_e32 v0, 0x800, v0
	v_mov_b32_e32 v2, v1
	s_andn2_b64 exec, exec, s[14:15]
	s_cbranch_execnz .LBB0_1975
.LBB0_1976:
	s_or_b64 exec, exec, s[12:13]
	s_add_i32 s99, s33, 1
	s_cmp_eq_u32 s99, s27
	s_cbranch_scc1 .Lmy_xpf_skip_1
	s_lshl_b32 s99, s99, 4
	v_or_b32_e32 v224, s99, v115
	v_ashrrev_i32_e32 v225, 31, v224
	v_lshlrev_b64 v[224:225], 13, v[224:225]
	v_lshl_add_u64 v[224:225], v[72:73], 0, v[224:225]
	global_load_dwordx4 v[160:163], v[224:225], off
	global_load_dwordx4 v[164:167], v[224:225], off offset:16
	global_load_dwordx4 v[168:171], v[224:225], off offset:128
	global_load_dwordx4 v[172:175], v[224:225], off offset:144
	global_load_dwordx4 v[176:179], v[224:225], off offset:256
	global_load_dwordx4 v[180:183], v[224:225], off offset:272
	global_load_dwordx4 v[184:187], v[224:225], off offset:384
	global_load_dwordx4 v[188:191], v[224:225], off offset:400
	global_load_dwordx4 v[192:195], v[224:225], off offset:512
	global_load_dwordx4 v[196:199], v[224:225], off offset:528
	global_load_dwordx4 v[200:203], v[224:225], off offset:640
	global_load_dwordx4 v[204:207], v[224:225], off offset:656
	global_load_dwordx4 v[208:211], v[224:225], off offset:768
	global_load_dwordx4 v[212:215], v[224:225], off offset:784
	global_load_dwordx4 v[216:219], v[224:225], off offset:896
	global_load_dwordx4 v[220:223], v[224:225], off offset:912
; #define LAS __attribute__((address_space(3)))
; template <int MODE>
; __device__ __forceinline__ void norm_phase(const MkArgs& a, LAS unsigned char* lds, const int l, const int wv) {
;     ...
;             if (tid < 16) {
;                 const LAS float* sl = lgt + tid * 36; const int tt = rb * 16 + tid;
;                 int grp = 0; float m = sl[0];
;                 for (int g = 1; g < 4; ++g) if (sl[g] > m) { m = sl[g]; grp = g; }
;                 float se = 0.f;
;                 for (int g = 0; g < 4; ++g) se += __builtin_amdgcn_exp2f((sl[g] - m) * 1.4426950408889634f);
;                 const float pg = 1.0f / se;
;                 const LAS float* lgp = sl + 4 + grp * 8;
;                 const f32x4 l0 = *(const LAS f32x4*)lgp, l1 = *(const LAS f32x4*)(lgp + 4);
;                 const float lv[8] = {l0[0], l0[1], l0[2], l0[3], l1[0], l1[1], l1[2], l1[3]};
;                 int i0 = 0; float v0 = lv[0];
; #pragma unroll
;                 for (int jx = 1; jx < 8; ++jx) if (lv[jx] > v0) { v0 = lv[jx]; i0 = jx; }
;                 int i1 = -1; float v1 = 0.f;
; #pragma unroll
;                 for (int jx = 0; jx < 8; ++jx) if (jx != i0 && (i1 < 0 || lv[jx] > v1)) { v1 = lv[jx]; i1 = jx; }
;                 const float e1 = __builtin_amdgcn_exp2f((v1 - v0) * 1.4426950408889634f);
;                 const float p0 = 1.0f / (1.0f + e1), p1 = e1 / (1.0f + e1);
;                 float* tokw = (float*)(ws + WS_TOKW);
;                 tokw[2 * tt] = pg * p0; tokw[2 * tt + 1] = pg * p1;
;                 const int ai = ((rb & 3) * 16 + tid) * 2;
;                 rexp[ai] = grp * 8 + i0; rexp[ai + 1] = grp * 8 + i1;
.Lmy_xpf_skip_1:
	s_waitcnt lgkmcnt(0)
	s_barrier
	s_and_saveexec_b64 s[20:21], s[8:9]
	s_cbranch_execz .LBB0_1978
	ds_read_b128 v[0:3], v122 offset:25600
	s_waitcnt lgkmcnt(0)
	v_cmp_gt_f32_e32 vcc, v1, v0
	s_nop 1
	v_cndmask_b32_e32 v4, v0, v1, vcc
	v_cmp_gt_f32_e64 s[12:13], v2, v4
	s_nop 1
	v_cndmask_b32_e64 v4, v4, v2, s[12:13]
	v_cmp_gt_f32_e64 s[14:15], v3, v4
	s_nop 1
	v_cndmask_b32_e64 v8, v4, v3, s[14:15]
	v_sub_f32_e32 v0, v0, v8
	v_sub_f32_e32 v1, v1, v8
	v_mul_f32_e32 v0, 0x3fb8aa3b, v0
	v_exp_f32_e32 v9, v0
	v_mul_f32_e32 v0, 0x3fb8aa3b, v1
	v_exp_f32_e32 v10, v0
	v_sub_f32_e32 v0, v2, v8
	v_mul_f32_e32 v0, 0x3fb8aa3b, v0
	v_exp_f32_e32 v11, v0
	v_cndmask_b32_e64 v0, 0, 8, vcc
	v_cndmask_b32_e64 v0, v0, 16, s[12:13]
	v_cndmask_b32_e64 v12, v0, 24, s[14:15]
	v_lshl_add_u32 v0, v12, 2, v122
	ds_read_b128 v[4:7], v0 offset:25616
	v_sub_f32_e32 v1, v3, v8
	v_mul_f32_e32 v1, 0x3fb8aa3b, v1
	v_exp_f32_e32 v8, v1
	ds_read_b128 v[0:3], v0 offset:25632
	s_waitcnt lgkmcnt(1)
	v_cmp_gt_f32_e32 vcc, v5, v4
	v_add_f32_e32 v9, 0, v9
	v_add_f32_e32 v9, v10, v9
	v_cndmask_b32_e32 v14, v4, v5, vcc
	v_cmp_gt_f32_e64 s[12:13], v6, v14
	v_cndmask_b32_e64 v13, 0, 1, vcc
	v_add_f32_e32 v9, v11, v9
	v_cndmask_b32_e64 v14, v14, v6, s[12:13]
	v_cndmask_b32_e64 v13, v13, 2, s[12:13]
	v_cmp_gt_f32_e64 s[12:13], v7, v14
	v_add_f32_e32 v8, v8, v9
	s_nop 0
	v_cndmask_b32_e64 v14, v14, v7, s[12:13]
	v_cndmask_b32_e64 v13, v13, 3, s[12:13]
	s_waitcnt lgkmcnt(0)
	v_cmp_gt_f32_e64 s[12:13], v0, v14
	s_nop 1
	v_cndmask_b32_e64 v14, v14, v0, s[12:13]
	v_cndmask_b32_e64 v13, v13, 4, s[12:13]
	v_cmp_gt_f32_e64 s[12:13], v1, v14
	s_nop 1
	v_cndmask_b32_e64 v14, v14, v1, s[12:13]
	v_cndmask_b32_e64 v13, v13, 5, s[12:13]
	v_cmp_gt_f32_e64 s[12:13], v2, v14
	s_nop 1
	v_cndmask_b32_e64 v14, v14, v2, s[12:13]
	v_cndmask_b32_e64 v13, v13, 6, s[12:13]
	v_cmp_ngt_f32_e64 s[14:15], v3, v14
	s_nop 1
	v_cndmask_b32_e64 v13, 7, v13, s[14:15]
	v_cmp_eq_u32_e64 s[16:17], 0, v13
	v_cmp_ne_u32_e64 s[18:19], 1, v13
	s_or_b64 s[16:17], s[16:17], vcc
	s_and_b64 vcc, s[18:19], s[16:17]
	v_cndmask_b32_e32 v4, v4, v5, vcc
	v_cndmask_b32_e64 v9, 0, 1, vcc
	v_cmp_gt_f32_e32 vcc, v6, v4
	s_nop 1
	v_cndmask_b32_e64 v5, v9, 2, vcc
	v_cndmask_b32_e32 v6, v4, v6, vcc
	v_cmp_eq_u32_e32 vcc, 2, v13
	s_nop 1
	v_cndmask_b32_e32 v4, v6, v4, vcc
	v_cndmask_b32_e32 v9, v5, v9, vcc
	v_cmp_gt_f32_e32 vcc, v7, v4
	s_nop 1
	v_cndmask_b32_e64 v9, v9, 3, vcc
	v_cndmask_b32_e32 v4, v4, v7, vcc
	v_cmp_eq_u32_e32 vcc, 3, v13
	s_nop 1
	v_cndmask_b32_e32 v6, v4, v6, vcc
	v_cndmask_b32_e32 v5, v9, v5, vcc
	v_cmp_gt_f32_e32 vcc, v0, v6
	s_nop 1
	v_cndmask_b32_e64 v5, v5, 4, vcc
	v_cndmask_b32_e32 v0, v6, v0, vcc
	v_cmp_eq_u32_e32 vcc, 4, v13
	s_nop 1
	v_cndmask_b32_e32 v4, v0, v4, vcc
	v_cndmask_b32_e32 v6, v5, v9, vcc
	v_cmp_gt_f32_e32 vcc, v1, v4
	s_nop 1
	v_cndmask_b32_e64 v6, v6, 5, vcc
	v_cndmask_b32_e32 v1, v4, v1, vcc
	v_cmp_eq_u32_e32 vcc, 5, v13
	s_nop 1
	v_cndmask_b32_e32 v0, v1, v0, vcc
	v_cndmask_b32_e32 v4, v6, v5, vcc
	v_cmp_gt_f32_e32 vcc, v2, v0
	s_nop 1
	v_cndmask_b32_e64 v1, v4, 6, vcc
	v_cndmask_b32_e32 v2, v0, v2, vcc
	s_and_b64 vcc, s[12:13], s[14:15]
	v_div_scale_f32 v5, s[12:13], v8, v8, 1.0
	v_cndmask_b32_e32 v0, v2, v0, vcc
	v_rcp_f32_e32 v6, v5
	v_cndmask_b32_e32 v4, v1, v4, vcc
	v_cmp_gt_f32_e32 vcc, v3, v0
	s_nop 1
	v_cndmask_b32_e64 v2, v4, 7, vcc
	s_and_b64 vcc, s[14:15], vcc
	v_cndmask_b32_e64 v4, v3, v14, s[14:15]
	v_cndmask_b32_e32 v0, v0, v3, vcc
	v_cndmask_b32_e64 v7, v1, v2, s[14:15]
	v_fma_f32 v1, -v5, v6, 1.0
	v_sub_f32_e32 v0, v0, v4
	v_fmac_f32_e32 v6, v1, v6
	v_div_scale_f32 v1, vcc, 1.0, v8, 1.0
	v_mul_f32_e32 v0, 0x3fb8aa3b, v0
	v_mul_f32_e32 v2, v1, v6
	v_exp_f32_e32 v4, v0
	v_fma_f32 v3, -v5, v2, v1
	v_fmac_f32_e32 v2, v3, v6
	v_fma_f32 v1, -v5, v2, v1
	v_div_fmas_f32 v0, v1, v6, v2
	v_add_f32_e32 v1, 1.0, v4
	v_div_scale_f32 v5, s[12:13], v1, v1, v4
	v_rcp_f32_e32 v6, v5
	v_div_fixup_f32 v0, v0, v8, 1.0
	v_add_lshl_u32 v2, s1, v64, 1
	v_ashrrev_i32_e32 v3, 31, v2
	v_fma_f32 v8, -v5, v6, 1.0
	v_fmac_f32_e32 v6, v8, v6
	v_div_scale_f32 v8, vcc, v4, v1, v4
	v_mul_f32_e32 v9, v8, v6
	v_fma_f32 v10, -v5, v9, v8
	v_fmac_f32_e32 v9, v10, v6
	v_fma_f32 v5, -v5, v9, v8
	v_div_scale_f32 v8, s[12:13], v1, v1, 1.0
	v_rcp_f32_e32 v10, v8
	v_div_fmas_f32 v5, v5, v6, v9
	v_div_fixup_f32 v5, v5, v1, v4
	v_lshl_add_u64 v[2:3], v[2:3], 2, s[24:25]
	v_fma_f32 v4, -v8, v10, 1.0
	v_fmac_f32_e32 v10, v4, v10
	v_div_scale_f32 v4, vcc, 1.0, v1, 1.0
	v_mul_f32_e32 v6, v4, v10
	v_fma_f32 v9, -v8, v6, v4
	v_fmac_f32_e32 v6, v9, v10
	v_fma_f32 v4, -v8, v6, v4
	v_div_fmas_f32 v4, v4, v10, v6
	v_div_fixup_f32 v4, v4, v1, 1.0
	v_pk_mul_f32 v[0:1], v[0:1], v[4:5] op_sel_hi:[0,1]
	s_and_b32 s1, s1, 48
	global_store_dwordx2 v[2:3], v[0:1], off
	v_add_u32_e32 v1, s1, v64
	v_or_b32_e32 v0, v13, v12
	v_lshl_add_u32 v2, v1, 3, 0
	v_add_u32_e32 v1, v7, v12
	ds_write_b64 v2, v[0:1] offset:28672
